# MoE GEMM phases: block->expert table staged in spare LDS once per phase; per-unit lookup reads LDS instead of global load + vmcnt(0)
# baseline (speedup 1.0000x reference)
.LBB0_2855:
	s_or_b64 exec, exec, s[0:1]
	v_mov_b32_e32 v10, v0
	s_waitcnt lgkmcnt(0)
	v_mov_b32_e32 v1, s76
	v_mov_b32_e32 v2, s77
	s_barrier
	v_mov_b32_e32 v3, 0x5a0000
	v_readfirstlane_b32 s4, v1
	v_mov_b32_e32 v1, s78
	v_readfirstlane_b32 s5, v2
	v_mov_b32_e32 v1, s74
	v_mov_b32_e32 v2, s75
	s_add_u32 s33, s4, 0x5a0000
	s_nop 1
	global_load_dword v3, v3, s[4:5] offset:640
	v_readfirstlane_b32 s30, v1
	s_addc_u32 s34, s5, 0
	v_readfirstlane_b32 s31, v2
	v_readfirstlane_b32 s1, v10
	s_waitcnt vmcnt(0)
	v_readfirstlane_b32 s35, v3
	v_cmp_gt_u32_e32 vcc, 0xa0, v0
	s_and_saveexec_b64 s[98:99], vcc
	v_lshlrev_b32_e32 v1, 2, v0
	v_add_u32_e32 v2, 0x5a0000, v1
	global_load_dword v2, v2, s[4:5]
	v_add_u32_e32 v1, 0x20000, v1
	s_waitcnt vmcnt(0)
	ds_write_b32 v1, v2
	s_mov_b64 exec, s[98:99]
	s_waitcnt lgkmcnt(0)
	s_barrier
	s_mul_i32 s0, s35, 28
	s_cmp_ge_i32 s30, s0
	s_cbranch_scc0 .LBB0_2858
	s_sub_i32 s6, s30, s0
	s_cmp_lt_i32 s6, 0
	s_mov_b64 s[2:3], 0
	s_cbranch_scc1 .LBB0_2859
	s_mov_b64 s[6:7], 0
	s_and_b64 vcc, exec, s[2:3]
	s_cbranch_vccnz .LBB0_2860
	s_branch .LBB0_2865

.LBB0_2874:
	s_mov_b64 s[16:17], 0
	s_andn2_b64 vcc, exec, s[18:19]
	s_mov_b64 s[28:29], 0
	s_cbranch_vccnz .LBB0_2876
	s_sub_i32 s12, 0, s5
	s_lshr_b32 s12, s12, 2
	s_mul_hi_u32 s13, s12, 0x24924925
	s_sub_i32 s12, s35, s13
	s_mul_i32 s13, s13, 28
	s_add_i32 s14, s13, s5
	s_ashr_i32 s13, s12, 31
	s_lshl_b64 s[18:19], s[12:13], 2
	s_add_u32 s18, s33, s18
	s_addc_u32 s19, s34, s19
	s_lshl_b32 s98, s12, 2
	s_add_i32 s98, s98, 0x20000
	v_mov_b32_e32 v2, s98
	ds_read_b32 v2, v2
	s_mov_b64 s[28:29], -1
	s_waitcnt lgkmcnt(0)
	v_readfirstlane_b32 s54, v2

.LBB0_2881:
	s_ashr_i32 s4, s12, 3
	s_add_i32 s4, s14, s4
	s_mul_hi_i32 s5, s4, 0x92492493
	s_add_i32 s5, s5, s4
	s_lshr_b32 s12, s5, 31
	s_ashr_i32 s5, s5, 6
	s_add_i32 s5, s5, s12
	s_lshl_b32 s12, s5, 2
	s_sub_i32 s13, s35, s12
	s_min_i32 s13, s13, 4
	s_abs_i32 s14, s13
	v_cvt_f32_u32_e32 v2, s14
	s_sub_i32 s16, 0, s14
	s_mulk_i32 s5, 0x70
	s_sub_i32 s4, s4, s5
	v_rcp_iflag_f32_e32 v2, v2
	s_abs_i32 s5, s4
	s_xor_b32 s15, s4, s13
	s_ashr_i32 s15, s15, 31
	v_mul_f32_e32 v2, 0x4f7ffffe, v2
	v_cvt_u32_f32_e32 v2, v2
	s_mov_b64 s[28:29], -1
	v_readfirstlane_b32 s17, v2
	s_mul_i32 s16, s16, s17
	s_mul_hi_u32 s16, s17, s16
	s_add_i32 s17, s17, s16
	s_mul_hi_u32 s16, s5, s17
	s_mul_i32 s17, s16, s14
	s_sub_i32 s5, s5, s17
	s_add_i32 s18, s16, 1
	s_sub_i32 s17, s5, s14
	s_cmp_ge_u32 s5, s14
	s_cselect_b32 s16, s18, s16
	s_cselect_b32 s5, s17, s5
	s_add_i32 s17, s16, 1
	s_cmp_ge_u32 s5, s14
	s_cselect_b32 s5, s17, s16
	s_xor_b32 s5, s5, s15
	s_sub_i32 s14, s5, s15
	s_mul_i32 s5, s14, s13
	s_sub_i32 s4, s4, s5
	s_add_i32 s12, s12, s4
	s_ashr_i32 s13, s12, 31
	s_lshl_b64 s[4:5], s[12:13], 2
	s_add_u32 s4, s33, s4
	s_addc_u32 s5, s34, s5
	s_lshl_b32 s98, s12, 2
	s_add_i32 s98, s98, 0x20000
	v_mov_b32_e32 v2, s98
	ds_read_b32 v2, v2
	s_waitcnt lgkmcnt(0)
	v_readfirstlane_b32 s54, v2

.LBB0_2946:
	s_or_b64 exec, exec, s[0:1]
	v_mov_b32_e32 v10, v0
	s_waitcnt lgkmcnt(0)
	v_mov_b32_e32 v1, s76
	v_mov_b32_e32 v2, s77
	s_barrier
	v_mov_b32_e32 v3, 0x5a0000
	v_readfirstlane_b32 s2, v1
	v_mov_b32_e32 v1, s78
	v_readfirstlane_b32 s3, v2
	v_mov_b32_e32 v1, s74
	v_mov_b32_e32 v2, s75
	s_mov_b32 s33, 1
	s_nop 1
	global_load_dword v3, v3, s[2:3] offset:640
	v_readfirstlane_b32 s30, v1
	v_readfirstlane_b32 s31, v2
	s_waitcnt vmcnt(0)
	v_readfirstlane_b32 s0, v3
	v_cmp_gt_u32_e32 vcc, 0xa0, v0
	s_and_saveexec_b64 s[98:99], vcc
	v_lshlrev_b32_e32 v1, 2, v0
	v_add_u32_e32 v2, 0x5a0000, v1
	global_load_dword v2, v2, s[2:3]
	v_add_u32_e32 v1, 0x20000, v1
	s_waitcnt vmcnt(0)
	ds_write_b32 v1, v2
	s_mov_b64 exec, s[98:99]
	s_waitcnt lgkmcnt(0)
	s_barrier
	s_and_b32 s1, s0, 63
	s_cmp_lt_u32 s1, 33
	s_cselect_b32 s4, 2, 1
	s_cmp_gt_u32 s1, 16
	s_cselect_b32 s4, s4, 4
	s_cmp_gt_u32 s1, 9
	s_cselect_b32 s4, s4, 7
	s_cmp_lg_u32 s1, 0
	s_cselect_b32 s4, s4, 1
	s_cmp_lg_u32 s4, 1
	s_cselect_b32 s12, s1, 0
	s_cmp_eq_u32 s12, 0
	s_mov_b32 s1, 0
	s_cbranch_scc1 .LBB0_2948
	v_cvt_f32_ubyte0_e32 v1, s4
	v_rcp_iflag_f32_e32 v2, v1
	s_mov_b32 s5, 0x42600000
	s_lshl_b32 s1, s12, 2
	s_mov_b32 s33, s4
	v_mul_f32_e32 v2, 0x42600000, v2
	v_trunc_f32_e32 v2, v2
	v_cvt_u32_f32_e32 v3, v2
	v_fma_f32 v2, -v2, v1, s5
	v_cmp_ge_f32_e64 s[6:7], |v2|, v1
	s_cmp_lg_u64 s[6:7], 0
	v_readfirstlane_b32 s5, v3
	s_addc_u32 s5, s5, 0
	s_and_b32 s34, s5, 63
	s_branch .LBB0_2949

.LBB0_2965:
	s_add_i32 s49, s49, 1
	s_mul_i32 s0, s49, s54
	s_mul_hi_u32 s1, s49, s31
	s_add_i32 s1, s1, s0
	s_mul_i32 s0, s49, s31
	s_add_u32 s0, s0, s30
	s_addc_u32 s1, s1, s55
	v_cmp_lt_i64_e32 vcc, s[0:1], v[142:143]
	s_mov_b64 s[20:21], -1
	s_cbranch_vccnz .LBB0_2968
	s_sub_i32 s1, s0, s6
	s_mov_b64 s[20:21], 0
	s_cmp_ge_i32 s1, s38
	s_mov_b64 s[18:19], 0
	s_cbranch_scc1 .LBB0_2968
	s_abs_i32 s15, s1
	s_mul_hi_u32 s16, s15, s60
	s_mul_i32 s17, s16, s33
	s_sub_i32 s15, s15, s17
	s_ashr_i32 s14, s1, 31
	s_add_i32 s17, s16, 1
	s_sub_i32 s18, s15, s33
	s_cmp_ge_u32 s15, s33
	s_cselect_b32 s16, s17, s16
	s_cselect_b32 s15, s18, s15
	s_add_i32 s17, s16, 1
	s_cmp_ge_u32 s15, s33
	s_cselect_b32 s15, s17, s16
	s_xor_b32 s15, s15, s14
	s_sub_i32 s15, s15, s14
	s_mul_i32 s14, s15, s33
	s_sub_i32 s63, s1, s14
	s_ashr_i32 s1, s15, 31
	s_lshr_b32 s1, s1, 30
	s_add_i32 s1, s15, s1
	s_ashr_i32 s14, s1, 2
	s_add_i32 s14, s14, s37
	s_and_b32 s1, s1, -4
	s_sub_i32 s62, s15, s1
	s_ashr_i32 s15, s14, 31
	s_lshl_b64 s[16:17], s[14:15], 2
	s_add_u32 s16, s35, s16
	s_addc_u32 s17, s36, s17
	s_lshl_b32 s98, s14, 2
	s_add_i32 s98, s98, 0x20000
	v_mov_b32_e32 v2, s98
	ds_read_b32 v2, v2
	s_mov_b64 s[18:19], -1
	s_mul_i32 s16, s63, s34
	s_mov_b32 s64, s34
	s_waitcnt lgkmcnt(0)
	v_readfirstlane_b32 s15, v2

.LBB0_2973:
	s_ashr_i32 s0, s14, 3
	s_add_i32 s0, s16, s0
	s_ashr_i32 s1, s0, 31
	s_lshr_b32 s1, s1, 28
	s_add_i32 s1, s0, s1
	s_ashr_i32 s14, s1, 4
	s_lshl_b32 s14, s14, 2
	s_sub_i32 s15, s37, s14
	s_min_i32 s15, s15, 4
	s_abs_i32 s16, s15
	v_cvt_f32_u32_e32 v2, s16
	s_sub_i32 s18, 0, s16
	s_and_b32 s1, s1, -16
	s_sub_i32 s0, s0, s1
	v_rcp_iflag_f32_e32 v2, v2
	s_abs_i32 s1, s0
	s_xor_b32 s17, s0, s15
	s_ashr_i32 s17, s17, 31
	v_mul_f32_e32 v2, 0x4f7ffffe, v2
	v_cvt_u32_f32_e32 v2, v2
	s_mov_b32 s64, 56
	s_mov_b32 s63, -1
	v_readfirstlane_b32 s19, v2
	s_mul_i32 s18, s18, s19
	s_mul_hi_u32 s18, s19, s18
	s_add_i32 s19, s19, s18
	s_mul_hi_u32 s18, s1, s19
	s_mul_i32 s19, s18, s16
	s_sub_i32 s1, s1, s19
	s_add_i32 s20, s18, 1
	s_sub_i32 s19, s1, s16
	s_cmp_ge_u32 s1, s16
	s_cselect_b32 s18, s20, s18
	s_cselect_b32 s1, s19, s1
	s_add_i32 s19, s18, 1
	s_cmp_ge_u32 s1, s16
	s_cselect_b32 s1, s19, s18
	s_xor_b32 s1, s1, s17
	s_sub_i32 s62, s1, s17
	s_mul_i32 s1, s62, s15
	s_sub_i32 s0, s0, s1
	s_add_i32 s14, s14, s0
	s_ashr_i32 s15, s14, 31
	s_lshl_b64 s[0:1], s[14:15], 2
	s_add_u32 s0, s35, s0
	s_addc_u32 s1, s36, s1
	s_lshl_b32 s98, s14, 2
	s_add_i32 s98, s98, 0x20000
	v_mov_b32_e32 v2, s98
	ds_read_b32 v2, v2
	s_mov_b32 s16, 0
	s_mov_b64 s[18:19], -1
	s_waitcnt lgkmcnt(0)
	v_readfirstlane_b32 s15, v2

.LBB0_5755:
	s_or_b64 exec, exec, s[0:1]
	v_readlane_b32 s0, v243, 8
	v_readlane_b32 s1, v243, 9
	v_mov_b32_e32 v10, v0
	s_waitcnt lgkmcnt(0)
	v_mov_b32_e32 v1, s0
	v_mov_b32_e32 v2, s1
	s_barrier
	v_mov_b32_e32 v3, 0x5a0000
	v_readfirstlane_b32 s0, v1
	v_mov_b32_e32 v1, s79
	v_readfirstlane_b32 s1, v2
	v_mov_b32_e32 v1, s77
	v_mov_b32_e32 v2, s78
	s_add_u32 s33, s0, 0x5a0000
	s_nop 1
	global_load_dword v3, v3, s[0:1] offset:640
	v_readfirstlane_b32 s30, v1
	s_addc_u32 s34, s1, 0
	v_readfirstlane_b32 s31, v2
	v_readfirstlane_b32 s3, v10
	s_waitcnt vmcnt(0)
	v_readfirstlane_b32 s35, v3
	v_cmp_gt_u32_e32 vcc, 0xa0, v0
	s_and_saveexec_b64 s[98:99], vcc
	v_lshlrev_b32_e32 v1, 2, v0
	v_add_u32_e32 v2, 0x5a0000, v1
	global_load_dword v2, v2, s[0:1]
	v_add_u32_e32 v1, 0x20000, v1
	s_waitcnt vmcnt(0)
	ds_write_b32 v1, v2
	s_mov_b64 exec, s[98:99]
	s_waitcnt lgkmcnt(0)
	s_barrier
	s_mul_i32 s2, s35, 28
	s_cmp_ge_i32 s30, s2
	s_cbranch_scc0 .LBB0_5758
	s_sub_i32 s6, s30, s2
	s_cmp_lt_i32 s6, 0
	s_mov_b64 s[4:5], 0
	s_cbranch_scc1 .LBB0_5759
	s_mov_b64 s[6:7], 0
	s_and_b64 vcc, exec, s[4:5]
	s_cbranch_vccnz .LBB0_5760
	s_branch .LBB0_5765

.LBB0_5774:
	s_mov_b64 s[16:17], 0
	s_andn2_b64 vcc, exec, s[18:19]
	s_mov_b64 s[28:29], 0
	s_cbranch_vccnz .LBB0_5776
	s_sub_i32 s12, 0, s1
	s_lshr_b32 s12, s12, 2
	s_mul_hi_u32 s13, s12, 0x24924925
	s_sub_i32 s12, s35, s13
	s_mul_i32 s13, s13, 28
	s_add_i32 s14, s13, s1
	s_ashr_i32 s13, s12, 31
	s_lshl_b64 s[18:19], s[12:13], 2
	s_add_u32 s18, s33, s18
	s_addc_u32 s19, s34, s19
	s_lshl_b32 s98, s12, 2
	s_add_i32 s98, s98, 0x20000
	v_mov_b32_e32 v2, s98
	ds_read_b32 v2, v2
	s_mov_b64 s[28:29], -1
	s_waitcnt lgkmcnt(0)
	v_readfirstlane_b32 s54, v2

.LBB0_5781:
	s_ashr_i32 s0, s12, 3
	s_add_i32 s0, s14, s0
	s_mul_hi_i32 s1, s0, 0x92492493
	s_add_i32 s1, s1, s0
	s_lshr_b32 s12, s1, 31
	s_ashr_i32 s1, s1, 6
	s_add_i32 s1, s1, s12
	s_lshl_b32 s12, s1, 2
	s_sub_i32 s13, s35, s12
	s_min_i32 s13, s13, 4
	s_abs_i32 s14, s13
	v_cvt_f32_u32_e32 v2, s14
	s_sub_i32 s16, 0, s14
	s_mulk_i32 s1, 0x70
	s_sub_i32 s0, s0, s1
	v_rcp_iflag_f32_e32 v2, v2
	s_abs_i32 s1, s0
	s_xor_b32 s15, s0, s13
	s_ashr_i32 s15, s15, 31
	v_mul_f32_e32 v2, 0x4f7ffffe, v2
	v_cvt_u32_f32_e32 v2, v2
	s_mov_b64 s[28:29], -1
	v_readfirstlane_b32 s17, v2
	s_mul_i32 s16, s16, s17
	s_mul_hi_u32 s16, s17, s16
	s_add_i32 s17, s17, s16
	s_mul_hi_u32 s16, s1, s17
	s_mul_i32 s17, s16, s14
	s_sub_i32 s1, s1, s17
	s_add_i32 s18, s16, 1
	s_sub_i32 s17, s1, s14
	s_cmp_ge_u32 s1, s14
	s_cselect_b32 s16, s18, s16
	s_cselect_b32 s1, s17, s1
	s_add_i32 s17, s16, 1
	s_cmp_ge_u32 s1, s14
	s_cselect_b32 s1, s17, s16
	s_xor_b32 s1, s1, s15
	s_sub_i32 s14, s1, s15
	s_mul_i32 s1, s14, s13
	s_sub_i32 s0, s0, s1
	s_add_i32 s12, s12, s0
	s_ashr_i32 s13, s12, 31
	s_lshl_b64 s[0:1], s[12:13], 2
	s_add_u32 s0, s33, s0
	s_addc_u32 s1, s34, s1
	s_lshl_b32 s98, s12, 2
	s_add_i32 s98, s98, 0x20000
	v_mov_b32_e32 v2, s98
	ds_read_b32 v2, v2
	s_waitcnt lgkmcnt(0)
	v_readfirstlane_b32 s54, v2

.LBB0_5846:
	s_or_b64 exec, exec, s[0:1]
	v_readlane_b32 s0, v243, 8
	v_readlane_b32 s1, v243, 9
	v_mov_b32_e32 v10, v0
	s_waitcnt lgkmcnt(0)
	v_mov_b32_e32 v1, s0
	v_mov_b32_e32 v2, s1
	s_barrier
	v_mov_b32_e32 v3, 0x5a0000
	v_readfirstlane_b32 s2, v1
	v_mov_b32_e32 v1, s79
	v_readfirstlane_b32 s3, v2
	v_mov_b32_e32 v1, s77
	v_mov_b32_e32 v2, s78
	s_mov_b32 s33, 1
	s_nop 1
	global_load_dword v3, v3, s[2:3] offset:640
	v_readfirstlane_b32 s30, v1
	v_readfirstlane_b32 s31, v2
	s_waitcnt vmcnt(0)
	v_readfirstlane_b32 s0, v3
	v_cmp_gt_u32_e32 vcc, 0xa0, v0
	s_and_saveexec_b64 s[98:99], vcc
	v_lshlrev_b32_e32 v1, 2, v0
	v_add_u32_e32 v2, 0x5a0000, v1
	global_load_dword v2, v2, s[2:3]
	v_add_u32_e32 v1, 0x20000, v1
	s_waitcnt vmcnt(0)
	ds_write_b32 v1, v2
	s_mov_b64 exec, s[98:99]
	s_waitcnt lgkmcnt(0)
	s_barrier
	s_and_b32 s1, s0, 63
	s_cmp_lt_u32 s1, 33
	s_cselect_b32 s4, 2, 1
	s_cmp_gt_u32 s1, 16
	s_cselect_b32 s4, s4, 4
	s_cmp_gt_u32 s1, 9
	s_cselect_b32 s4, s4, 7
	s_cmp_lg_u32 s1, 0
	s_cselect_b32 s4, s4, 1
	s_cmp_lg_u32 s4, 1
	s_cselect_b32 s10, s1, 0
	s_cmp_eq_u32 s10, 0
	s_mov_b32 s1, 0
	s_cbranch_scc1 .LBB0_5848
	v_cvt_f32_ubyte0_e32 v1, s4
	v_rcp_iflag_f32_e32 v2, v1
	s_mov_b32 s5, 0x42600000
	s_lshl_b32 s1, s10, 2
	s_mov_b32 s33, s4
	v_mul_f32_e32 v2, 0x42600000, v2
	v_trunc_f32_e32 v2, v2
	v_cvt_u32_f32_e32 v3, v2
	v_fma_f32 v2, -v2, v1, s5
	v_cmp_ge_f32_e64 s[6:7], |v2|, v1
	s_cmp_lg_u64 s[6:7], 0
	v_readfirstlane_b32 s5, v3
	s_addc_u32 s5, s5, 0
	s_and_b32 s34, s5, 63
	s_branch .LBB0_5849

.LBB0_5865:
	s_add_i32 s49, s49, 1
	s_mul_i32 s0, s49, s54
	s_mul_hi_u32 s1, s49, s31
	s_add_i32 s1, s1, s0
	s_mul_i32 s0, s49, s31
	s_add_u32 s0, s0, s30
	s_addc_u32 s1, s1, s55
	v_cmp_lt_i64_e32 vcc, s[0:1], v[142:143]
	s_mov_b64 s[20:21], -1
	s_cbranch_vccnz .LBB0_5868
	s_sub_i32 s1, s0, s4
	s_mov_b64 s[20:21], 0
	s_cmp_ge_i32 s1, s38
	s_mov_b64 s[16:17], 0
	s_cbranch_scc1 .LBB0_5868
	s_abs_i32 s13, s1
	s_mul_hi_u32 s14, s13, s60
	s_mul_i32 s15, s14, s33
	s_sub_i32 s13, s13, s15
	s_ashr_i32 s12, s1, 31
	s_add_i32 s15, s14, 1
	s_sub_i32 s16, s13, s33
	s_cmp_ge_u32 s13, s33
	s_cselect_b32 s14, s15, s14
	s_cselect_b32 s13, s16, s13
	s_add_i32 s15, s14, 1
	s_cmp_ge_u32 s13, s33
	s_cselect_b32 s13, s15, s14
	s_xor_b32 s13, s13, s12
	s_sub_i32 s13, s13, s12
	s_mul_i32 s12, s13, s33
	s_sub_i32 s63, s1, s12
	s_ashr_i32 s1, s13, 31
	s_lshr_b32 s1, s1, 30
	s_add_i32 s1, s13, s1
	s_ashr_i32 s12, s1, 2
	s_add_i32 s12, s12, s37
	s_and_b32 s1, s1, -4
	s_sub_i32 s62, s13, s1
	s_ashr_i32 s13, s12, 31
	s_lshl_b64 s[14:15], s[12:13], 2
	s_add_u32 s14, s35, s14
	s_addc_u32 s15, s36, s15
	s_lshl_b32 s98, s12, 2
	s_add_i32 s98, s98, 0x20000
	v_mov_b32_e32 v2, s98
	ds_read_b32 v2, v2
	s_mov_b64 s[16:17], -1
	s_mul_i32 s14, s63, s34
	s_mov_b32 s64, s34
	s_waitcnt lgkmcnt(0)
	v_readfirstlane_b32 s13, v2

.LBB0_5873:
	s_ashr_i32 s0, s12, 3
	s_add_i32 s0, s14, s0
	s_ashr_i32 s1, s0, 31
	s_lshr_b32 s1, s1, 28
	s_add_i32 s1, s0, s1
	s_ashr_i32 s12, s1, 4
	s_lshl_b32 s12, s12, 2
	s_sub_i32 s13, s37, s12
	s_min_i32 s13, s13, 4
	s_abs_i32 s14, s13
	v_cvt_f32_u32_e32 v2, s14
	s_sub_i32 s16, 0, s14
	s_and_b32 s1, s1, -16
	s_sub_i32 s0, s0, s1
	v_rcp_iflag_f32_e32 v2, v2
	s_abs_i32 s1, s0
	s_xor_b32 s15, s0, s13
	s_ashr_i32 s15, s15, 31
	v_mul_f32_e32 v2, 0x4f7ffffe, v2
	v_cvt_u32_f32_e32 v2, v2
	s_mov_b32 s64, 56
	s_mov_b32 s63, -1
	v_readfirstlane_b32 s17, v2
	s_mul_i32 s16, s16, s17
	s_mul_hi_u32 s16, s17, s16
	s_add_i32 s17, s17, s16
	s_mul_hi_u32 s16, s1, s17
	s_mul_i32 s17, s16, s14
	s_sub_i32 s1, s1, s17
	s_add_i32 s20, s16, 1
	s_sub_i32 s17, s1, s14
	s_cmp_ge_u32 s1, s14
	s_cselect_b32 s16, s20, s16
	s_cselect_b32 s1, s17, s1
	s_add_i32 s17, s16, 1
	s_cmp_ge_u32 s1, s14
	s_cselect_b32 s1, s17, s16
	s_xor_b32 s1, s1, s15
	s_sub_i32 s62, s1, s15
	s_mul_i32 s1, s62, s13
	s_sub_i32 s0, s0, s1
	s_add_i32 s12, s12, s0
	s_ashr_i32 s13, s12, 31
	s_lshl_b64 s[0:1], s[12:13], 2
	s_add_u32 s0, s35, s0
	s_addc_u32 s1, s36, s1
	s_lshl_b32 s98, s12, 2
	s_add_i32 s98, s98, 0x20000
	v_mov_b32_e32 v2, s98
	ds_read_b32 v2, v2
	s_mov_b32 s14, 0
	s_mov_b64 s[16:17], -1
	s_waitcnt lgkmcnt(0)
	v_readfirstlane_b32 s13, v2
